# baseline (speedup 1.0000x reference)
_Z6k_gemmPKfS0_PK15HIP_vector_typeIjLj4EEPDF16_PKh:
	s_load_dwordx4 s[20:23], s[0:1], 0x0
	s_load_dwordx4 s[4:7], s[0:1], 0x10
	s_load_dwordx2 s[38:39], s[0:1], 0x20
	v_readfirstlane_b32 s8, v0
	v_and_b32_e32 v1, 63, v0
	s_nop 3
	s_lshr_b32 s8, s8, 6
	s_and_b32 s40, s2, 7
	s_lshr_b32 s41, s2, 3
	s_mul_i32 s18, s40, 0x187
	s_add_u32 s19, s18, 0x187
	s_min_u32 s19, s19, 0xc35
	s_sub_u32 s33, s19, s18
	s_sub_u32 s33, s33, 0x180
	s_lshl_b32 s33, s33, 2
	s_cmp_lt_u32 s41, s33
	s_cselect_b32 s44, 7, 6
	s_lshr_b32 s45, s41, 2
	s_add_u32 s45, s45, s18
	s_add_u32 s45, s45, 0x180
	s_lshl_b32 s45, s45, 4
	s_and_b32 s46, s41, 3
	s_lshl_b32 s46, s46, 2
	s_add_u32 s47, s45, s46
	s_mul_i32 s45, s47, 0x4b0
	s_lshl_b32 s46, s47, 8
	s_add_i32 s18, s18, s41
	s_cmp_eq_u32 s8, 0
	s_cselect_b32 s9, s44, 6
	s_add_i32 s11, s44, 4
	s_lshl_b32 s18, s18, 4
	s_lshl_b32 s19, s8, 2
	s_add_i32 s33, s18, s19
	s_mul_i32 s12, s33, 0x4b0
	s_lshl_b32 s32, s18, 8
	s_sub_u32 s32, s32, 0x100000
	s_mov_b32 s10, 0
	v_lshl_add_u32 v253, v1, 10, s33
	v_mov_b32_e32 v254, s47
	v_cmp_eq_u32_e32 vcc, 6, v1
	s_nop 1
	v_cndmask_b32_e32 v253, v253, v254, vcc
	v_mov_b32_e32 v247, 0
	v_cmp_gt_i32_e32 vcc, s9, v1
	s_mov_b32 s18, 0xc350
	v_cmp_gt_i32_e64 s[36:37], s18, v253
	s_and_b64 vcc, vcc, s[36:37]
	s_waitcnt lgkmcnt(0)
	s_and_saveexec_b64 s[36:37], vcc
	global_load_dword v247, v253, s[38:39]
	s_mov_b64 exec, s[36:37]
	s_mov_b32 s24, s22
	s_and_b32 s25, s23, 0xffff
	s_mov_b32 s26, 0x3938700
	s_mov_b32 s27, 0x20000
	s_and_b32 s21, s21, 0xffff
	s_mov_b32 s22, 0x3938700
	s_mov_b32 s23, 0x20000
	s_mov_b32 s28, s6
	s_and_b32 s29, s7, 0xffff
	s_mov_b32 s30, 0xc35000
	s_mov_b32 s31, 0x20000
	v_lshlrev_b32_e32 v238, 4, v1
	v_mul_u32_u24_e32 v253, 0x1746, v1
	v_lshrrev_b32_e32 v253, 16, v253
	v_min_u32_e32 v253, 3, v253
	v_mul_u32_u24_e32 v254, 11, v253
	v_sub_u32_e32 v254, v1, v254
	v_lshlrev_b32_e32 v240, 3, v253
	v_mul_u32_u24_e32 v249, 0x4b0, v253
	v_lshl_add_u32 v249, v254, 4, v249
	v_add_u32_e32 v249, 0x400, v249
	v_mov_b32_e32 v255, 0x80000000
	v_cmp_gt_u32_e64 s[34:35], 44, v1
	s_nop 1
	v_cndmask_b32_e64 v239, v255, v249, s[34:35]
	v_lshl_add_u32 v250, s8, 2, v253
	v_mul_u32_u24_e32 v250, 0x4e0, v250
	v_lshl_add_u32 v250, v254, 3, v250
	v_add_u32_e32 v242, 0x200, v250
	s_mul_i32 s18, s8, 0x1380
	v_lshl_add_u32 v241, v1, 3, s18
	v_and_b32_e32 v249, 15, v1
	v_lshrrev_b32_e32 v250, 4, v1
	v_mul_u32_u24_e32 v243, 0x4e0, v249
	v_lshl_add_u32 v243, v250, 4, v243
	v_mul_u32_u24_e32 v244, 0x440, v250
	v_lshl_add_u32 v244, v249, 1, v244
	s_lshl_b32 s18, s8, 6
	s_add_i32 s18, s18, 39936
	v_add_u32_e32 v244, s18, v244
	v_lshrrev_b32_e32 v249, 4, v0
	v_and_b32_e32 v250, 15, v0
	v_mul_u32_u24_e32 v245, 0x110, v249
	v_lshl_add_u32 v245, v250, 4, v245
	v_add_u32_e32 v245, 39936, v245
	v_lshlrev_b32_e32 v246, 8, v249
	v_lshl_add_u32 v246, v250, 4, v246
	s_lshl_b32 s18, s8, 12
	s_add_i32 s18, s18, 48640
	v_lshl_add_u32 v248, v1, 4, s18
	v_cmp_gt_u32_e32 vcc, 32, v0
	s_and_saveexec_b64 s[36:37], vcc
	v_mul_u32_u24_e32 v251, 0x4e00, v249
	v_mul_u32_u24_e32 v252, 0x4e0, v250
	v_add_u32_e32 v254, v251, v252
	v_mov_b32_e32 v250, 0
	v_mov_b32_e32 v251, 0
	v_mov_b32_e32 v252, 0
	v_mov_b32_e32 v253, 0
	ds_write_b128 v254, v[250:253] offset:1200
	s_mov_b64 exec, s[36:37]
	s_lshl_b32 s18, s8, 11
	v_lshl_add_u32 v253, v1, 4, s18
	v_add_u32_e32 v254, 0x22000, v253
	global_load_dwordx4 v[178:181], v254, s[4:5]
	global_load_dwordx4 v[182:185], v254, s[4:5] offset:1024
	v_add_u32_e32 v254, 0x2000, v254
	global_load_dwordx4 v[186:189], v254, s[4:5]
	global_load_dwordx4 v[190:193], v254, s[4:5] offset:1024
	v_mov_b32_e32 v236, v253
	s_waitcnt vmcnt(4)
	v_readlane_b32 s13, v247, s10
	s_add_u32 s14, s12, 0x4b0
	s_add_u32 s15, s12, 0x960
	s_add_u32 s16, s12, 0xe10
	s_nop 1
	s_and_b32 s18, s13, 0xff
	s_cmp_eq_u32 s18, 1
	s_cselect_b32 s42, s12, 0x80000000
	s_and_b32 s18, s13, 0xff00
	s_cmp_eq_u32 s18, 0x100
	s_cselect_b32 s14, s14, 0x80000000
	s_and_b32 s18, s13, 0xff0000
	s_cmp_eq_u32 s18, 0x10000
	s_cselect_b32 s15, s15, 0x80000000
	s_and_b32 s18, s13, 0xff000000
	s_cmp_eq_u32 s18, 0x1000000
	s_cselect_b32 s16, s16, 0x80000000
	v_lshrrev_b32_e64 v249, v240, s13
	v_and_b32_e32 v249, 0xff, v249
	v_cmp_eq_u32_e32 vcc, 1, v249
	s_nop 1
	v_cndmask_b32_e32 v254, v255, v239, vcc
	buffer_load_dwordx4 v[138:141], v238, s[20:23], s42 offen sc0 nt
	buffer_load_dwordx4 v[142:145], v238, s[24:27], s42 offen sc0 nt
	buffer_load_dwordx4 v[146:149], v238, s[20:23], s14 offen sc0 nt
	buffer_load_dwordx4 v[150:153], v238, s[24:27], s14 offen sc0 nt
	buffer_load_dwordx4 v[154:157], v238, s[20:23], s15 offen sc0 nt
	buffer_load_dwordx4 v[158:161], v238, s[24:27], s15 offen sc0 nt
	buffer_load_dwordx4 v[162:165], v238, s[20:23], s16 offen sc0 nt
	buffer_load_dwordx4 v[166:169], v238, s[24:27], s16 offen sc0 nt
	buffer_load_dwordx4 v[170:173], v254, s[20:23], s12 offen sc0 nt
	buffer_load_dwordx4 v[174:177], v254, s[24:27], s12 offen sc0 nt
	s_add_u32 s12, s12, 0x12c000
	s_add_u32 s32, s32, 0x40000
	s_mov_b32 s19, 0x80000000
	buffer_store_dwordx4 v[226:229], v246, s[28:31], s19 offen sc0 sc1
	s_mov_b32 s10, 1
	global_load_dwordx4 v[2:5], v236, s[4:5]
	global_load_dwordx4 v[6:9], v236, s[4:5] offset:1024
	v_add_u32_e32 v236, 0x2000, v236
	global_load_dwordx4 v[10:13], v236, s[4:5]
	global_load_dwordx4 v[14:17], v236, s[4:5] offset:1024
	v_add_u32_e32 v236, 0x2000, v236
	global_load_dwordx4 v[18:21], v236, s[4:5]
	global_load_dwordx4 v[22:25], v236, s[4:5] offset:1024
	v_add_u32_e32 v236, 0x2000, v236
	global_load_dwordx4 v[26:29], v236, s[4:5]
	global_load_dwordx4 v[30:33], v236, s[4:5] offset:1024
	v_add_u32_e32 v236, 0x2000, v236
	global_load_dwordx4 v[34:37], v236, s[4:5]
	global_load_dwordx4 v[38:41], v236, s[4:5] offset:1024
	v_add_u32_e32 v236, 0x2000, v236
	global_load_dwordx4 v[42:45], v236, s[4:5]
	global_load_dwordx4 v[46:49], v236, s[4:5] offset:1024
	v_add_u32_e32 v236, 0x2000, v236
	global_load_dwordx4 v[50:53], v236, s[4:5]
	global_load_dwordx4 v[54:57], v236, s[4:5] offset:1024
	v_add_u32_e32 v236, 0x2000, v236
	global_load_dwordx4 v[58:61], v236, s[4:5]
	global_load_dwordx4 v[62:65], v236, s[4:5] offset:1024
	v_add_u32_e32 v236, 0x2000, v236
	global_load_dwordx4 v[66:69], v236, s[4:5]
	global_load_dwordx4 v[70:73], v236, s[4:5] offset:1024
	v_add_u32_e32 v236, 0x2000, v236
	global_load_dwordx4 v[74:77], v236, s[4:5]
	global_load_dwordx4 v[78:81], v236, s[4:5] offset:1024
	v_add_u32_e32 v236, 0x2000, v236
	global_load_dwordx4 v[82:85], v236, s[4:5]
	global_load_dwordx4 v[86:89], v236, s[4:5] offset:1024
	v_add_u32_e32 v236, 0x2000, v236
	global_load_dwordx4 v[90:93], v236, s[4:5]
	global_load_dwordx4 v[94:97], v236, s[4:5] offset:1024
	v_add_u32_e32 v236, 0x2000, v236
	global_load_dwordx4 v[98:101], v236, s[4:5]
	global_load_dwordx4 v[102:105], v236, s[4:5] offset:1024
	v_add_u32_e32 v236, 0x2000, v236
	global_load_dwordx4 v[106:109], v236, s[4:5]
	global_load_dwordx4 v[110:113], v236, s[4:5] offset:1024
	v_add_u32_e32 v236, 0x2000, v236
	global_load_dwordx4 v[114:117], v236, s[4:5]
	global_load_dwordx4 v[118:121], v236, s[4:5] offset:1024
	v_add_u32_e32 v236, 0x2000, v236
	global_load_dwordx4 v[122:125], v236, s[4:5]
	global_load_dwordx4 v[126:129], v236, s[4:5] offset:1024
	v_add_u32_e32 v236, 0x2000, v236
	global_load_dwordx4 v[130:133], v236, s[4:5]
	global_load_dwordx4 v[134:137], v236, s[4:5] offset:1024
	s_waitcnt vmcnt(45)
	ds_write_b128 v248, v[178:181]
	ds_write_b128 v248, v[182:185] offset:1024
	ds_write_b128 v248, v[186:189] offset:2048
	ds_write_b128 v248, v[190:193] offset:3072
	s_waitcnt lgkmcnt(0)
	s_barrier
	s_branch .Lg_half1

.Lg_noprep0:
	s_sub_u32 s18, s10, 2
	s_cmp_lt_u32 s18, s9
	s_cbranch_scc0 .Lg_s2skip0
	s_cmp_gt_u32 s10, s9
	s_cbranch_scc1 .Lg_s2finalb0
	s_cmp_eq_u32 s10, s9
	s_cbranch_scc1 .Lg_s2final0
	s_waitcnt vmcnt(21)
	v_cvt_pk_f16_f32 v250, v138, v139
	v_cvt_pk_f16_f32 v251, v140, v141
	ds_write_b64 v241, v[250:251] offset:0
	buffer_load_dwordx4 v[138:141], v238, s[20:23], s42 offen sc0 nt
	s_waitcnt vmcnt(21)
	v_cvt_pk_f16_f32 v252, v142, v143
	v_cvt_pk_f16_f32 v253, v144, v145
	ds_write_b64 v241, v[252:253] offset:600
	buffer_load_dwordx4 v[142:145], v238, s[24:27], s42 offen sc0 nt
	s_waitcnt vmcnt(21)
	v_cvt_pk_f16_f32 v250, v146, v147
	v_cvt_pk_f16_f32 v251, v148, v149
	ds_write_b64 v241, v[250:251] offset:1248
	buffer_load_dwordx4 v[146:149], v238, s[20:23], s14 offen sc0 nt
	s_waitcnt vmcnt(21)
	v_cvt_pk_f16_f32 v252, v150, v151
	v_cvt_pk_f16_f32 v253, v152, v153
	ds_write_b64 v241, v[252:253] offset:1848
	buffer_load_dwordx4 v[150:153], v238, s[24:27], s14 offen sc0 nt
	s_waitcnt vmcnt(21)
	v_cvt_pk_f16_f32 v250, v154, v155
	v_cvt_pk_f16_f32 v251, v156, v157
	ds_write_b64 v241, v[250:251] offset:2496
	buffer_load_dwordx4 v[154:157], v238, s[20:23], s15 offen sc0 nt
	s_waitcnt vmcnt(21)
	v_cvt_pk_f16_f32 v252, v158, v159
	v_cvt_pk_f16_f32 v253, v160, v161
	ds_write_b64 v241, v[252:253] offset:3096
	buffer_load_dwordx4 v[158:161], v238, s[24:27], s15 offen sc0 nt
	s_waitcnt vmcnt(21)
	v_cvt_pk_f16_f32 v250, v162, v163
	v_cvt_pk_f16_f32 v251, v164, v165
	ds_write_b64 v241, v[250:251] offset:3744
	buffer_load_dwordx4 v[162:165], v238, s[20:23], s16 offen sc0 nt
	s_waitcnt vmcnt(21)
	v_cvt_pk_f16_f32 v252, v166, v167
	v_cvt_pk_f16_f32 v253, v168, v169
	ds_write_b64 v241, v[252:253] offset:4344
	buffer_load_dwordx4 v[166:169], v238, s[24:27], s16 offen sc0 nt
	s_mov_b64 exec, s[34:35]
	s_waitcnt vmcnt(21)
	v_cvt_pk_f16_f32 v250, v170, v171
	v_cvt_pk_f16_f32 v251, v172, v173
	ds_write_b64 v242, v[250:251] offset:0
	s_mov_b64 exec, -1
	buffer_load_dwordx4 v[170:173], v254, s[20:23], s12 offen sc0 nt
	s_mov_b64 exec, s[34:35]
	s_waitcnt vmcnt(21)
	v_cvt_pk_f16_f32 v252, v174, v175
	v_cvt_pk_f16_f32 v253, v176, v177
	ds_write_b64 v242, v[252:253] offset:600
	s_mov_b64 exec, -1
	buffer_load_dwordx4 v[174:177], v254, s[24:27], s12 offen sc0 nt
	s_branch .Lg_s1done0

.Lg_s2skip0:
	s_cmp_ge_u32 s10, s9
	s_cbranch_scc1 .Lg_s1done0
	buffer_load_dwordx4 v[138:141], v238, s[20:23], s42 offen sc0 nt
	buffer_load_dwordx4 v[142:145], v238, s[24:27], s42 offen sc0 nt
	buffer_load_dwordx4 v[146:149], v238, s[20:23], s14 offen sc0 nt
	buffer_load_dwordx4 v[150:153], v238, s[24:27], s14 offen sc0 nt
	buffer_load_dwordx4 v[154:157], v238, s[20:23], s15 offen sc0 nt
	buffer_load_dwordx4 v[158:161], v238, s[24:27], s15 offen sc0 nt
	buffer_load_dwordx4 v[162:165], v238, s[20:23], s16 offen sc0 nt
	buffer_load_dwordx4 v[166:169], v238, s[24:27], s16 offen sc0 nt
	buffer_load_dwordx4 v[170:173], v254, s[20:23], s12 offen sc0 nt
	buffer_load_dwordx4 v[174:177], v254, s[24:27], s12 offen sc0 nt

.Lg_noprep1:
	s_sub_u32 s18, s10, 2
	s_cmp_lt_u32 s18, s9
	s_cbranch_scc0 .Lg_s2skip1
	s_cmp_gt_u32 s10, s9
	s_cbranch_scc1 .Lg_s2finalb1
	s_cmp_eq_u32 s10, s9
	s_cbranch_scc1 .Lg_s2final1
	s_waitcnt vmcnt(21)
	v_cvt_pk_f16_f32 v250, v178, v179
	v_cvt_pk_f16_f32 v251, v180, v181
	ds_write_b64 v241, v[250:251] offset:19968
	buffer_load_dwordx4 v[178:181], v238, s[20:23], s42 offen sc0 nt
	s_waitcnt vmcnt(21)
	v_cvt_pk_f16_f32 v252, v182, v183
	v_cvt_pk_f16_f32 v253, v184, v185
	ds_write_b64 v241, v[252:253] offset:20568
	buffer_load_dwordx4 v[182:185], v238, s[24:27], s42 offen sc0 nt
	s_waitcnt vmcnt(21)
	v_cvt_pk_f16_f32 v250, v186, v187
	v_cvt_pk_f16_f32 v251, v188, v189
	ds_write_b64 v241, v[250:251] offset:21216
	buffer_load_dwordx4 v[186:189], v238, s[20:23], s14 offen sc0 nt
	s_waitcnt vmcnt(21)
	v_cvt_pk_f16_f32 v252, v190, v191
	v_cvt_pk_f16_f32 v253, v192, v193
	ds_write_b64 v241, v[252:253] offset:21816
	buffer_load_dwordx4 v[190:193], v238, s[24:27], s14 offen sc0 nt
	s_waitcnt vmcnt(21)
	v_cvt_pk_f16_f32 v250, v194, v195
	v_cvt_pk_f16_f32 v251, v196, v197
	ds_write_b64 v241, v[250:251] offset:22464
	buffer_load_dwordx4 v[194:197], v238, s[20:23], s15 offen sc0 nt
	s_waitcnt vmcnt(21)
	v_cvt_pk_f16_f32 v252, v198, v199
	v_cvt_pk_f16_f32 v253, v200, v201
	ds_write_b64 v241, v[252:253] offset:23064
	buffer_load_dwordx4 v[198:201], v238, s[24:27], s15 offen sc0 nt
	s_waitcnt vmcnt(21)
	v_cvt_pk_f16_f32 v250, v202, v203
	v_cvt_pk_f16_f32 v251, v204, v205
	ds_write_b64 v241, v[250:251] offset:23712
	buffer_load_dwordx4 v[202:205], v238, s[20:23], s16 offen sc0 nt
	s_waitcnt vmcnt(21)
	v_cvt_pk_f16_f32 v252, v206, v207
	v_cvt_pk_f16_f32 v253, v208, v209
	ds_write_b64 v241, v[252:253] offset:24312
	buffer_load_dwordx4 v[206:209], v238, s[24:27], s16 offen sc0 nt
	s_mov_b64 exec, s[34:35]
	s_waitcnt vmcnt(21)
	v_cvt_pk_f16_f32 v250, v210, v211
	v_cvt_pk_f16_f32 v251, v212, v213
	ds_write_b64 v242, v[250:251] offset:19968
	s_mov_b64 exec, -1
	buffer_load_dwordx4 v[210:213], v254, s[20:23], s12 offen sc0 nt
	s_mov_b64 exec, s[34:35]
	s_waitcnt vmcnt(21)
	v_cvt_pk_f16_f32 v252, v214, v215
	v_cvt_pk_f16_f32 v253, v216, v217
	ds_write_b64 v242, v[252:253] offset:20568
	s_mov_b64 exec, -1
	buffer_load_dwordx4 v[214:217], v254, s[24:27], s12 offen sc0 nt
	s_branch .Lg_s1done1

.Lg_s2skip1:
	s_cmp_ge_u32 s10, s9
	s_cbranch_scc1 .Lg_s1done1
	buffer_load_dwordx4 v[178:181], v238, s[20:23], s42 offen sc0 nt
	buffer_load_dwordx4 v[182:185], v238, s[24:27], s42 offen sc0 nt
	buffer_load_dwordx4 v[186:189], v238, s[20:23], s14 offen sc0 nt
	buffer_load_dwordx4 v[190:193], v238, s[24:27], s14 offen sc0 nt
	buffer_load_dwordx4 v[194:197], v238, s[20:23], s15 offen sc0 nt
	buffer_load_dwordx4 v[198:201], v238, s[24:27], s15 offen sc0 nt
	buffer_load_dwordx4 v[202:205], v238, s[20:23], s16 offen sc0 nt
	buffer_load_dwordx4 v[206:209], v238, s[24:27], s16 offen sc0 nt
	buffer_load_dwordx4 v[210:213], v254, s[20:23], s12 offen sc0 nt
	buffer_load_dwordx4 v[214:217], v254, s[24:27], s12 offen sc0 nt
